# in-loop K/V/G projection: all W fragments prefetched into idle score registers, counted lgkmcnt, MFMA stream no longer paced by just-in-time LDS reads
# baseline (speedup 1.0000x reference)
.LBB1_59:
	s_setprio 0
	s_nop 10
	v_rcp_f32_e32 v8, v82
	v_cvt_f32_f16_sdwa v5, v229 dst_sel:DWORD dst_unused:UNUSED_PAD src0_sel:WORD_1
	v_cvt_f32_f16_e32 v4, v229
	v_cvt_f32_f16_sdwa v7, v230 dst_sel:DWORD dst_unused:UNUSED_PAD src0_sel:WORD_1
	v_cvt_f32_f16_e32 v6, v230
	v_cvt_f32_f16_sdwa v11, v232 dst_sel:DWORD dst_unused:UNUSED_PAD src0_sel:WORD_1
	v_cvt_f32_f16_e32 v10, v232
	v_cvt_f32_f16_sdwa v13, v234 dst_sel:DWORD dst_unused:UNUSED_PAD src0_sel:WORD_1
	v_cvt_f32_f16_e32 v12, v234
	v_pk_mul_f32 v[4:5], v[8:9], v[4:5] op_sel_hi:[0,1]
	v_pk_mul_f32 v[6:7], v[8:9], v[6:7] op_sel_hi:[0,1]
	v_pk_mul_f32 v[4:5], v[98:99], v[4:5]
	v_pk_mul_f32 v[6:7], v[100:101], v[6:7]
	v_cvt_pk_f16_f32 v4, v4, v5
	v_cvt_pk_f16_f32 v5, v6, v7
	v_pk_mul_f32 v[6:7], v[8:9], v[10:11] op_sel_hi:[0,1]
	v_pk_mul_f32 v[10:11], v[8:9], v[12:13] op_sel_hi:[0,1]
	v_pk_mul_f32 v[6:7], v[102:103], v[6:7]
	v_pk_mul_f32 v[10:11], v[104:105], v[10:11]
	v_cvt_pk_f16_f32 v6, v6, v7
	v_cvt_pk_f16_f32 v7, v10, v11
	v_cvt_f32_f16_sdwa v11, v228 dst_sel:DWORD dst_unused:UNUSED_PAD src0_sel:WORD_1
	v_cvt_f32_f16_e32 v10, v228
	ds_write_b128 v227, v[4:7]
	v_cvt_f32_f16_sdwa v7, v231 dst_sel:DWORD dst_unused:UNUSED_PAD src0_sel:WORD_1
	v_cvt_f32_f16_e32 v6, v231
	v_pk_mul_f32 v[4:5], v[8:9], v[10:11] op_sel_hi:[0,1]
	v_cvt_f32_f16_sdwa v11, v233 dst_sel:DWORD dst_unused:UNUSED_PAD src0_sel:WORD_1
	v_cvt_f32_f16_e32 v10, v233
	v_cvt_f32_f16_sdwa v13, v235 dst_sel:DWORD dst_unused:UNUSED_PAD src0_sel:WORD_1
	v_cvt_f32_f16_e32 v12, v235
	v_pk_mul_f32 v[6:7], v[8:9], v[6:7] op_sel_hi:[0,1]
	v_pk_mul_f32 v[4:5], v[4:5], v[106:107]
	v_pk_mul_f32 v[6:7], v[6:7], v[108:109]
	v_cvt_pk_f16_f32 v4, v4, v5
	v_cvt_pk_f16_f32 v5, v6, v7
	v_pk_mul_f32 v[6:7], v[8:9], v[10:11] op_sel_hi:[0,1]
	v_pk_mul_f32 v[8:9], v[8:9], v[12:13] op_sel_hi:[0,1]
	v_pk_mul_f32 v[6:7], v[6:7], v[110:111]
	v_pk_mul_f32 v[8:9], v[8:9], v[112:113]
	v_cvt_pk_f16_f32 v6, v6, v7
	v_cvt_pk_f16_f32 v7, v8, v9
	s_and_b64 vcc, exec, s[16:17]
	ds_write_b128 v227, v[4:7] offset:1024
	s_waitcnt vmcnt(0) lgkmcnt(0)
	s_barrier
	s_cbranch_vccnz .LBB1_5
	ds_read_b128 v[18:21], v206 offset:8192
	ds_read_b128 v[50:53], v206 offset:16384
	ds_read_b128 v[22:25], v206 offset:9216
	ds_read_b128 v[54:57], v206 offset:17408
	ds_read_b128 v[26:29], v206 offset:10240
	ds_read_b128 v[58:61], v206 offset:18432
	ds_read_b128 v[30:33], v206 offset:11264
	ds_read_b128 v[62:65], v206 offset:19456
	ds_read_b128 v[34:37], v206 offset:12288
	ds_read_b128 v[66:69], v206 offset:20480
	ds_read_b128 v[38:41], v206 offset:13312
	ds_read_b128 v[70:73], v206 offset:21504
	ds_read_b128 v[42:45], v206 offset:14336
	ds_read_b128 v[74:77], v206 offset:22528
	s_waitcnt lgkmcnt(13)
	v_mfma_f32_32x32x16_f16 v[114:129], v[18:21], v[130:133], 0
	s_waitcnt lgkmcnt(12)
	v_mfma_f32_32x32x16_f16 v[98:113], v[130:133], v[50:53], 0
	ds_read_b128 v[46:49], v206 offset:15360
	ds_read_b128 v[78:81], v206 offset:23552
	s_waitcnt lgkmcnt(13)
	v_mfma_f32_32x32x16_f16 v[114:129], v[22:25], v[134:137], v[114:129]
	s_waitcnt lgkmcnt(12)
	v_mfma_f32_32x32x16_f16 v[98:113], v[134:137], v[54:57], v[98:113]
	ds_read_b128 v[18:21], v206 offset:24576
	s_waitcnt lgkmcnt(12)
	v_mfma_f32_32x32x16_f16 v[114:129], v[26:29], v[138:141], v[114:129]
	s_waitcnt lgkmcnt(11)
	v_mfma_f32_32x32x16_f16 v[98:113], v[138:141], v[58:61], v[98:113]
	ds_read_b128 v[50:53], v206 offset:25600
	s_waitcnt lgkmcnt(11)
	v_mfma_f32_32x32x16_f16 v[114:129], v[30:33], v[142:145], v[114:129]
	s_waitcnt lgkmcnt(10)
	v_mfma_f32_32x32x16_f16 v[98:113], v[142:145], v[62:65], v[98:113]
	ds_read_b128 v[22:25], v206 offset:26624
	s_waitcnt lgkmcnt(10)
	v_mfma_f32_32x32x16_f16 v[114:129], v[34:37], v[146:149], v[114:129]
	s_waitcnt lgkmcnt(9)
	v_mfma_f32_32x32x16_f16 v[98:113], v[146:149], v[66:69], v[98:113]
	ds_read_b128 v[54:57], v206 offset:27648
	s_waitcnt lgkmcnt(9)
	v_mfma_f32_32x32x16_f16 v[114:129], v[38:41], v[150:153], v[114:129]
	s_waitcnt lgkmcnt(8)
	v_mfma_f32_32x32x16_f16 v[98:113], v[150:153], v[70:73], v[98:113]
	ds_read_b128 v[26:29], v206 offset:28672
	s_waitcnt lgkmcnt(8)
	v_mfma_f32_32x32x16_f16 v[114:129], v[42:45], v[154:157], v[114:129]
	s_waitcnt lgkmcnt(7)
	v_mfma_f32_32x32x16_f16 v[98:113], v[154:157], v[74:77], v[98:113]
	ds_read_b128 v[58:61], v206 offset:29696
	s_waitcnt lgkmcnt(7)
	v_mfma_f32_32x32x16_f16 v[114:129], v[46:49], v[158:161], v[114:129]
	s_waitcnt lgkmcnt(6)
	v_mfma_f32_32x32x16_f16 v[98:113], v[158:161], v[78:81], v[98:113]
	ds_read_b128 v[30:33], v206 offset:30720
	global_load_dwordx4 v[4:7], v[220:221], off
	s_waitcnt lgkmcnt(6)
	v_mfma_f32_32x32x16_f16 v[82:97], v[18:21], v[130:133], 0
	s_waitcnt lgkmcnt(5)
	v_mfma_f32_32x32x16_f16 v[82:97], v[50:53], v[134:137], v[82:97]
	s_waitcnt lgkmcnt(4)
	v_mfma_f32_32x32x16_f16 v[82:97], v[22:25], v[138:141], v[82:97]
	s_waitcnt lgkmcnt(3)
	v_mfma_f32_32x32x16_f16 v[82:97], v[54:57], v[142:145], v[82:97]
	s_waitcnt lgkmcnt(2)
	v_mfma_f32_32x32x16_f16 v[82:97], v[26:29], v[146:149], v[82:97]
	s_waitcnt lgkmcnt(1)
	v_mfma_f32_32x32x16_f16 v[82:97], v[58:61], v[150:153], v[82:97]
	s_waitcnt lgkmcnt(0)
	v_mfma_f32_32x32x16_f16 v[82:97], v[30:33], v[154:157], v[82:97]
	v_cvt_pk_f16_f32 v121, v120, v121
	v_cvt_pk_f16_f32 v120, v118, v119
	v_cvt_pk_f16_f32 v119, v116, v117
	v_cvt_pk_f16_f32 v118, v114, v115
	v_cvt_pk_f16_f32 v117, v128, v129
	v_cvt_pk_f16_f32 v116, v126, v127
	v_cvt_pk_f16_f32 v115, v124, v125
	v_cvt_pk_f16_f32 v114, v122, v123
	ds_write_b128 v209, v[114:117] offset:33792
	global_load_dwordx4 v[114:117], v[220:221], off offset:96
	ds_write_b128 v209, v[118:121] offset:32768
	v_cvt_pk_f16_f32 v105, v104, v105
	v_cvt_pk_f16_f32 v104, v102, v103
	v_cvt_pk_f16_f32 v103, v100, v101
	v_cvt_pk_f16_f32 v102, v98, v99
	ds_write_b128 v209, v[102:105] offset:49152
	global_load_dwordx4 v[8:11], v[220:221], off offset:32
	v_cvt_pk_f16_f32 v103, v108, v109
	v_cvt_pk_f16_f32 v102, v106, v107
	v_cvt_pk_f16_f32 v105, v112, v113
	v_cvt_pk_f16_f32 v104, v110, v111
	ds_write_b128 v209, v[102:105] offset:50176
	global_load_dwordx4 v[12:15], v[220:221], off offset:64
	ds_read_b128 v[106:109], v206 offset:31744
	ds_read_b128 v[98:101], v206
	ds_read_b128 v[118:121], v206 offset:1024
	ds_read_b128 v[122:125], v206 offset:2048
	ds_read_b128 v[126:129], v206 offset:3072
	ds_read_b128 v[196:199], v206 offset:4096
	ds_read_b128 v[200:203], v206 offset:5120
	ds_read_b128 v[230:233], v206 offset:6144
	ds_read_b128 v[236:239], v206 offset:7168
	s_waitcnt lgkmcnt(0)
	s_barrier
	v_mfma_f32_32x32x16_f16 v[82:97], v[106:109], v[158:161], v[82:97]
	v_mfma_f32_32x32x16_f16 v[98:113], v[98:101], v[130:133], 0
	s_waitcnt vmcnt(3)
	s_nop 9
	v_add_f32_e32 v1, v82, v4
	v_mfma_f32_32x32x16_f16 v[98:113], v[118:121], v[134:137], v[98:113]
	v_add_f32_e32 v3, v5, v83
	v_add_f32_e32 v4, v6, v84
	v_add_f32_e32 v5, v7, v85
	v_mul_f32_e32 v1, 0xbfb8aa3b, v1
	v_mul_f32_e32 v3, 0xbfb8aa3b, v3
	v_mul_f32_e32 v4, 0xbfb8aa3b, v4
	v_mul_f32_e32 v5, 0xbfb8aa3b, v5
	v_mfma_f32_32x32x16_f16 v[98:113], v[122:125], v[138:141], v[98:113]
	v_exp_f32_e32 v1, v1
	v_exp_f32_e32 v3, v3
	v_exp_f32_e32 v4, v4
	v_exp_f32_e32 v5, v5
	v_add_f32_e32 v1, 1.0, v1
	v_add_f32_e32 v3, 1.0, v3
	v_add_f32_e32 v4, 1.0, v4
	v_mfma_f32_32x32x16_f16 v[98:113], v[126:129], v[142:145], v[98:113]
	v_add_f32_e32 v5, 1.0, v5
	s_waitcnt vmcnt(2)
	v_add_f32_e32 v16, v116, v96
	v_add_f32_e32 v17, v117, v97
	v_mul_f32_e32 v16, 0xbfb8aa3b, v16
	v_mul_f32_e32 v17, 0xbfb8aa3b, v17
	v_exp_f32_e32 v16, v16
	v_exp_f32_e32 v17, v17
	v_mfma_f32_32x32x16_f16 v[98:113], v[196:199], v[146:149], v[98:113]
	s_waitcnt vmcnt(1)
	v_add_f32_e32 v6, v86, v8
	v_add_f32_e32 v7, v9, v87
	v_add_f32_e32 v8, v10, v88
	v_add_f32_e32 v9, v11, v89
	v_mul_f32_e32 v6, 0xbfb8aa3b, v6
	v_mul_f32_e32 v7, 0xbfb8aa3b, v7
	v_mul_f32_e32 v8, 0xbfb8aa3b, v8
	v_mfma_f32_32x32x16_f16 v[98:113], v[200:203], v[150:153], v[98:113]
	s_waitcnt vmcnt(0)
	v_add_f32_e32 v10, v90, v12
	v_add_f32_e32 v11, v13, v91
	v_add_f32_e32 v12, v14, v92
	v_add_f32_e32 v13, v15, v93
	v_add_f32_e32 v14, v94, v114
	v_add_f32_e32 v15, v115, v95
	v_mul_f32_e32 v9, 0xbfb8aa3b, v9
	v_mfma_f32_32x32x16_f16 v[98:113], v[230:233], v[154:157], v[98:113]
	v_mul_f32_e32 v10, 0xbfb8aa3b, v10
	v_mul_f32_e32 v11, 0xbfb8aa3b, v11
	v_mul_f32_e32 v12, 0xbfb8aa3b, v12
	v_mul_f32_e32 v13, 0xbfb8aa3b, v13
	v_mul_f32_e32 v14, 0xbfb8aa3b, v14
	v_mul_f32_e32 v15, 0xbfb8aa3b, v15
	v_exp_f32_e32 v6, v6
	v_exp_f32_e32 v7, v7
	v_exp_f32_e32 v8, v8
	v_exp_f32_e32 v9, v9
	v_exp_f32_e32 v10, v10
	v_exp_f32_e32 v11, v11
	v_exp_f32_e32 v12, v12
	v_exp_f32_e32 v13, v13
	v_exp_f32_e32 v14, v14
	v_exp_f32_e32 v15, v15
	v_mfma_f32_32x32x16_f16 v[98:113], v[236:239], v[158:161], v[98:113]
	v_add_f32_e32 v6, 1.0, v6
	v_add_f32_e32 v7, 1.0, v7
	v_add_f32_e32 v8, 1.0, v8
	v_add_f32_e32 v9, 1.0, v9
	v_add_f32_e32 v10, 1.0, v10
	v_add_f32_e32 v11, 1.0, v11
	v_add_f32_e32 v12, 1.0, v12
	v_add_f32_e32 v13, 1.0, v13
	v_add_f32_e32 v14, 1.0, v14
	v_add_f32_e32 v15, 1.0, v15
	v_add_f32_e32 v16, 1.0, v16
	v_add_f32_e32 v17, 1.0, v17
	v_rcp_f32_e32 v1, v1
	v_rcp_f32_e32 v3, v3
	v_rcp_f32_e32 v4, v4
	v_rcp_f32_e32 v5, v5
	v_rcp_f32_e32 v6, v6
	v_rcp_f32_e32 v7, v7
	v_rcp_f32_e32 v8, v8
	v_rcp_f32_e32 v9, v9
	v_rcp_f32_e32 v10, v10
	v_rcp_f32_e32 v11, v11
	v_rcp_f32_e32 v12, v12
	v_rcp_f32_e32 v13, v13
	v_rcp_f32_e32 v14, v14
	v_rcp_f32_e32 v15, v15
	v_rcp_f32_e32 v16, v16
	v_rcp_f32_e32 v17, v17
	v_cvt_pk_f16_f32 v228, v10, v11
	v_cvt_pk_f16_f32 v231, v12, v13
	v_cvt_pk_f16_f32 v233, v14, v15
	v_cvt_pk_f16_f32 v235, v16, v17
	v_cvt_pk_f16_f32 v229, v1, v3
	v_cvt_pk_f16_f32 v230, v4, v5
	v_cvt_pk_f16_f32 v232, v6, v7
	v_cvt_pk_f16_f32 v234, v8, v9
	v_cvt_pk_f16_f32 v202, v106, v107
	v_cvt_pk_f16_f32 v203, v108, v109
	v_cvt_pk_f16_f32 v204, v110, v111
	v_cvt_pk_f16_f32 v205, v112, v113
	v_cvt_pk_f16_f32 v198, v98, v99
	v_cvt_pk_f16_f32 v199, v100, v101
	v_cvt_pk_f16_f32 v200, v102, v103
	v_cvt_pk_f16_f32 v201, v104, v105
	s_branch .LBB1_5
